# proj epilogue stores use SGPR base + 32-bit lane offset (one address dword per lane)
# speedup vs baseline: 1.0763x; 1.0042x over previous
.LBB0_245:
	v_and_b32_e32 v11, 0x7fffffff, v14
	v_mov_b64_e32 v[6:7], s[10:11]
	s_movk_i32 s21, 0x2600
	v_mad_u64_u32 v[6:7], s[48:49], v11, s21, v[6:7]
	v_lshlrev_b32_e32 v4, 3, v10
	v_lshl_add_u64 v[12:13], v[6:7], 0, s[6:7]
	v_ashrrev_i32_e32 v5, 31, v4
	v_lshl_add_u64 v[12:13], v[12:13], 0, s[16:17]
	v_lshl_add_u64 v[12:13], v[12:13], 0, v[4:5]
	v_subrev_u32_e32 v12, s10, v12
	global_store_dwordx2 v12, v[8:9], s[10:11]
	v_cndmask_b32_e64 v8, 0, 1, s[28:29]
	v_cmp_ne_u32_e64 s[6:7], 1, v8
	s_andn2_b64 vcc, exec, s[28:29]
	s_mov_b64 s[28:29], -1
	s_cbranch_vccnz .LBB0_247
	s_mov_b32 s28, 0x3e800000
	v_pk_mul_f32 v[12:13], v[160:161], s[28:29] op_sel_hi:[1,0]
	v_pk_mul_f32 v[16:17], v[156:157], s[28:29] op_sel_hi:[1,0]
	v_mov_b32_e32 v8, v2
	v_mov_b32_e32 v9, v2
	v_cvt_pk_fp8_f32 v8, v12, v13
	v_cvt_pk_fp8_f32 v9, v16, v17
	v_pk_mul_f32 v[12:13], v[162:163], s[28:29] op_sel_hi:[1,0]
	v_pk_mul_f32 v[16:17], v[158:159], s[28:29] op_sel_hi:[1,0]
	v_cvt_pk_fp8_f32 v8, v12, v13 op_sel:[0,0,1]
	v_cvt_pk_fp8_f32 v9, v16, v17 op_sel:[0,0,1]
	s_mov_b64 s[28:29], 0

.LBB0_251:
	v_lshl_add_u64 v[6:7], v[6:7], 0, s[28:29]
	v_lshl_add_u64 v[6:7], v[6:7], 0, s[16:17]
	v_lshl_add_u64 v[6:7], v[6:7], 0, v[4:5]
	s_and_b64 vcc, exec, s[6:7]
	s_mov_b64 s[28:29], -1
	v_subrev_u32_e32 v6, s10, v6
	global_store_dwordx2 v6, v[8:9], s[10:11] offset:128
	s_cbranch_vccnz .LBB0_253
	s_mov_b32 s28, 0x3e800000
	v_pk_mul_f32 v[6:7], v[88:89], s[28:29] op_sel_hi:[1,0]
	v_pk_mul_f32 v[12:13], v[84:85], s[28:29] op_sel_hi:[1,0]
	v_mov_b32_e32 v8, v2
	v_mov_b32_e32 v9, v2
	v_cvt_pk_fp8_f32 v8, v6, v7
	v_cvt_pk_fp8_f32 v9, v12, v13
	v_pk_mul_f32 v[6:7], v[90:91], s[28:29] op_sel_hi:[1,0]
	v_pk_mul_f32 v[12:13], v[86:87], s[28:29] op_sel_hi:[1,0]
	v_cvt_pk_fp8_f32 v8, v6, v7 op_sel:[0,0,1]
	v_cvt_pk_fp8_f32 v9, v12, v13 op_sel:[0,0,1]
	s_mov_b64 s[28:29], 0

.LBB0_257:
	v_add_u32_e32 v6, 16, v14
	v_and_b32_e32 v11, 0x7fffffff, v6
	v_mov_b64_e32 v[6:7], s[10:11]
	v_mad_u64_u32 v[6:7], s[48:49], v11, s21, v[6:7]
	v_lshl_add_u64 v[12:13], v[6:7], 0, s[28:29]
	v_lshl_add_u64 v[12:13], v[12:13], 0, s[16:17]
	v_lshl_add_u64 v[12:13], v[12:13], 0, v[4:5]
	s_and_b64 vcc, exec, s[6:7]
	s_mov_b64 s[28:29], -1
	v_subrev_u32_e32 v12, s10, v12
	global_store_dwordx2 v12, v[8:9], s[10:11]
	s_cbranch_vccnz .LBB0_259
	s_mov_b32 s28, 0x3e800000
	v_pk_mul_f32 v[12:13], v[152:153], s[28:29] op_sel_hi:[1,0]
	v_pk_mul_f32 v[16:17], v[148:149], s[28:29] op_sel_hi:[1,0]
	v_mov_b32_e32 v8, v2
	v_mov_b32_e32 v9, v2
	v_cvt_pk_fp8_f32 v8, v12, v13
	v_cvt_pk_fp8_f32 v9, v16, v17
	v_pk_mul_f32 v[12:13], v[154:155], s[28:29] op_sel_hi:[1,0]
	v_pk_mul_f32 v[16:17], v[150:151], s[28:29] op_sel_hi:[1,0]
	v_cvt_pk_fp8_f32 v8, v12, v13 op_sel:[0,0,1]
	v_cvt_pk_fp8_f32 v9, v16, v17 op_sel:[0,0,1]
	s_mov_b64 s[28:29], 0

.LBB0_263:
	v_lshl_add_u64 v[6:7], v[6:7], 0, s[28:29]
	v_lshl_add_u64 v[6:7], v[6:7], 0, s[16:17]
	v_lshl_add_u64 v[6:7], v[6:7], 0, v[4:5]
	s_and_b64 vcc, exec, s[6:7]
	s_mov_b64 s[28:29], -1
	v_subrev_u32_e32 v6, s10, v6
	global_store_dwordx2 v6, v[8:9], s[10:11] offset:128
	s_cbranch_vccnz .LBB0_265
	s_mov_b32 s28, 0x3e800000
	v_pk_mul_f32 v[6:7], v[80:81], s[28:29] op_sel_hi:[1,0]
	v_pk_mul_f32 v[12:13], v[76:77], s[28:29] op_sel_hi:[1,0]
	v_mov_b32_e32 v8, v2
	v_mov_b32_e32 v9, v2
	v_cvt_pk_fp8_f32 v8, v6, v7
	v_cvt_pk_fp8_f32 v9, v12, v13
	v_pk_mul_f32 v[6:7], v[82:83], s[28:29] op_sel_hi:[1,0]
	v_pk_mul_f32 v[12:13], v[78:79], s[28:29] op_sel_hi:[1,0]
	v_cvt_pk_fp8_f32 v8, v6, v7 op_sel:[0,0,1]
	v_cvt_pk_fp8_f32 v9, v12, v13 op_sel:[0,0,1]
	s_mov_b64 s[28:29], 0

.LBB0_269:
	v_add_u32_e32 v6, 32, v14
	v_and_b32_e32 v11, 0x7fffffff, v6
	v_mov_b64_e32 v[6:7], s[10:11]
	v_mad_u64_u32 v[6:7], s[48:49], v11, s21, v[6:7]
	v_lshl_add_u64 v[12:13], v[6:7], 0, s[28:29]
	v_lshl_add_u64 v[12:13], v[12:13], 0, s[16:17]
	v_lshl_add_u64 v[12:13], v[12:13], 0, v[4:5]
	s_and_b64 vcc, exec, s[6:7]
	s_mov_b64 s[28:29], -1
	v_subrev_u32_e32 v12, s10, v12
	global_store_dwordx2 v12, v[8:9], s[10:11]
	s_cbranch_vccnz .LBB0_271
	s_mov_b32 s28, 0x3e800000
	v_pk_mul_f32 v[12:13], v[144:145], s[28:29] op_sel_hi:[1,0]
	v_pk_mul_f32 v[16:17], v[140:141], s[28:29] op_sel_hi:[1,0]
	v_mov_b32_e32 v8, v2
	v_mov_b32_e32 v9, v2
	v_cvt_pk_fp8_f32 v8, v12, v13
	v_cvt_pk_fp8_f32 v9, v16, v17
	v_pk_mul_f32 v[12:13], v[146:147], s[28:29] op_sel_hi:[1,0]
	v_pk_mul_f32 v[16:17], v[142:143], s[28:29] op_sel_hi:[1,0]
	v_cvt_pk_fp8_f32 v8, v12, v13 op_sel:[0,0,1]
	v_cvt_pk_fp8_f32 v9, v16, v17 op_sel:[0,0,1]
	s_mov_b64 s[28:29], 0

.LBB0_275:
	v_lshl_add_u64 v[6:7], v[6:7], 0, s[28:29]
	v_lshl_add_u64 v[6:7], v[6:7], 0, s[16:17]
	v_lshl_add_u64 v[6:7], v[6:7], 0, v[4:5]
	s_and_b64 vcc, exec, s[6:7]
	s_mov_b64 s[28:29], -1
	v_subrev_u32_e32 v6, s10, v6
	global_store_dwordx2 v6, v[8:9], s[10:11] offset:128
	s_cbranch_vccnz .LBB0_277
	s_mov_b32 s28, 0x3e800000
	v_pk_mul_f32 v[6:7], v[72:73], s[28:29] op_sel_hi:[1,0]
	v_pk_mul_f32 v[12:13], v[68:69], s[28:29] op_sel_hi:[1,0]
	v_mov_b32_e32 v8, v2
	v_mov_b32_e32 v9, v2
	v_cvt_pk_fp8_f32 v8, v6, v7
	v_cvt_pk_fp8_f32 v9, v12, v13
	v_pk_mul_f32 v[6:7], v[74:75], s[28:29] op_sel_hi:[1,0]
	v_pk_mul_f32 v[12:13], v[70:71], s[28:29] op_sel_hi:[1,0]
	v_cvt_pk_fp8_f32 v8, v6, v7 op_sel:[0,0,1]
	v_cvt_pk_fp8_f32 v9, v12, v13 op_sel:[0,0,1]
	s_mov_b64 s[28:29], 0

.LBB0_281:
	v_add_u32_e32 v6, 48, v14
	v_and_b32_e32 v11, 0x7fffffff, v6
	v_mov_b64_e32 v[6:7], s[10:11]
	v_mad_u64_u32 v[6:7], s[48:49], v11, s21, v[6:7]
	v_lshl_add_u64 v[12:13], v[6:7], 0, s[28:29]
	v_lshl_add_u64 v[12:13], v[12:13], 0, s[16:17]
	v_lshl_add_u64 v[12:13], v[12:13], 0, v[4:5]
	s_and_b64 vcc, exec, s[6:7]
	s_mov_b64 s[28:29], -1
	v_subrev_u32_e32 v12, s10, v12
	global_store_dwordx2 v12, v[8:9], s[10:11]
	s_cbranch_vccnz .LBB0_283
	s_mov_b32 s28, 0x3e800000
	v_pk_mul_f32 v[12:13], v[136:137], s[28:29] op_sel_hi:[1,0]
	v_pk_mul_f32 v[16:17], v[132:133], s[28:29] op_sel_hi:[1,0]
	v_mov_b32_e32 v8, v2
	v_mov_b32_e32 v9, v2
	v_cvt_pk_fp8_f32 v8, v12, v13
	v_cvt_pk_fp8_f32 v9, v16, v17
	v_pk_mul_f32 v[12:13], v[138:139], s[28:29] op_sel_hi:[1,0]
	v_pk_mul_f32 v[16:17], v[134:135], s[28:29] op_sel_hi:[1,0]
	v_cvt_pk_fp8_f32 v8, v12, v13 op_sel:[0,0,1]
	v_cvt_pk_fp8_f32 v9, v16, v17 op_sel:[0,0,1]
	s_mov_b64 s[28:29], 0

.LBB0_287:
	v_lshl_add_u64 v[6:7], v[6:7], 0, s[28:29]
	v_lshl_add_u64 v[6:7], v[6:7], 0, s[16:17]
	v_lshl_add_u64 v[6:7], v[6:7], 0, v[4:5]
	s_and_b64 vcc, exec, s[6:7]
	s_mov_b64 s[28:29], -1
	v_subrev_u32_e32 v6, s10, v6
	global_store_dwordx2 v6, v[8:9], s[10:11] offset:128
	s_cbranch_vccnz .LBB0_289
	s_mov_b32 s28, 0x3e800000
	v_pk_mul_f32 v[6:7], v[64:65], s[28:29] op_sel_hi:[1,0]
	v_pk_mul_f32 v[12:13], v[60:61], s[28:29] op_sel_hi:[1,0]
	v_mov_b32_e32 v8, v2
	v_mov_b32_e32 v9, v2
	v_cvt_pk_fp8_f32 v8, v6, v7
	v_cvt_pk_fp8_f32 v9, v12, v13
	v_pk_mul_f32 v[6:7], v[66:67], s[28:29] op_sel_hi:[1,0]
	v_pk_mul_f32 v[12:13], v[62:63], s[28:29] op_sel_hi:[1,0]
	v_cvt_pk_fp8_f32 v8, v6, v7 op_sel:[0,0,1]
	v_cvt_pk_fp8_f32 v9, v12, v13 op_sel:[0,0,1]
	s_mov_b64 s[28:29], 0

.LBB0_293:
	v_add_u32_e32 v6, 0x80, v14
	v_and_b32_e32 v11, 0x7fffffff, v6
	v_mov_b64_e32 v[6:7], s[10:11]
	v_mad_u64_u32 v[6:7], s[48:49], v11, s21, v[6:7]
	v_lshl_add_u64 v[12:13], v[6:7], 0, s[28:29]
	v_lshl_add_u64 v[12:13], v[12:13], 0, s[16:17]
	v_lshl_add_u64 v[12:13], v[12:13], 0, v[4:5]
	s_and_b64 vcc, exec, s[6:7]
	s_mov_b64 s[28:29], -1
	v_subrev_u32_e32 v12, s10, v12
	global_store_dwordx2 v12, v[8:9], s[10:11]
	s_cbranch_vccnz .LBB0_295
	s_mov_b32 s28, 0x3e800000
	v_pk_mul_f32 v[12:13], v[128:129], s[28:29] op_sel_hi:[1,0]
	v_pk_mul_f32 v[16:17], v[124:125], s[28:29] op_sel_hi:[1,0]
	v_mov_b32_e32 v8, v2
	v_mov_b32_e32 v9, v2
	v_cvt_pk_fp8_f32 v8, v12, v13
	v_cvt_pk_fp8_f32 v9, v16, v17
	v_pk_mul_f32 v[12:13], v[130:131], s[28:29] op_sel_hi:[1,0]
	v_pk_mul_f32 v[16:17], v[126:127], s[28:29] op_sel_hi:[1,0]
	v_cvt_pk_fp8_f32 v8, v12, v13 op_sel:[0,0,1]
	v_cvt_pk_fp8_f32 v9, v16, v17 op_sel:[0,0,1]
	s_mov_b64 s[28:29], 0

.LBB0_299:
	v_lshl_add_u64 v[6:7], v[6:7], 0, s[28:29]
	v_lshl_add_u64 v[6:7], v[6:7], 0, s[16:17]
	v_lshl_add_u64 v[6:7], v[6:7], 0, v[4:5]
	s_and_b64 vcc, exec, s[6:7]
	s_mov_b64 s[28:29], -1
	v_subrev_u32_e32 v6, s10, v6
	global_store_dwordx2 v6, v[8:9], s[10:11] offset:128
	s_cbranch_vccnz .LBB0_301
	s_mov_b32 s28, 0x3e800000
	v_pk_mul_f32 v[6:7], v[56:57], s[28:29] op_sel_hi:[1,0]
	v_pk_mul_f32 v[12:13], v[52:53], s[28:29] op_sel_hi:[1,0]
	v_mov_b32_e32 v8, v2
	v_mov_b32_e32 v9, v2
	v_cvt_pk_fp8_f32 v8, v6, v7
	v_cvt_pk_fp8_f32 v9, v12, v13
	v_pk_mul_f32 v[6:7], v[58:59], s[28:29] op_sel_hi:[1,0]
	v_pk_mul_f32 v[12:13], v[54:55], s[28:29] op_sel_hi:[1,0]
	v_cvt_pk_fp8_f32 v8, v6, v7 op_sel:[0,0,1]
	v_cvt_pk_fp8_f32 v9, v12, v13 op_sel:[0,0,1]
	s_mov_b64 s[28:29], 0

.LBB0_305:
	v_add_u32_e32 v6, 0x90, v14
	v_and_b32_e32 v11, 0x7fffffff, v6
	v_mov_b64_e32 v[6:7], s[10:11]
	v_mad_u64_u32 v[6:7], s[48:49], v11, s21, v[6:7]
	v_lshl_add_u64 v[12:13], v[6:7], 0, s[28:29]
	v_lshl_add_u64 v[12:13], v[12:13], 0, s[16:17]
	v_lshl_add_u64 v[12:13], v[12:13], 0, v[4:5]
	s_and_b64 vcc, exec, s[6:7]
	s_mov_b64 s[28:29], -1
	v_subrev_u32_e32 v12, s10, v12
	global_store_dwordx2 v12, v[8:9], s[10:11]
	s_cbranch_vccnz .LBB0_307
	s_mov_b32 s28, 0x3e800000
	v_pk_mul_f32 v[12:13], v[120:121], s[28:29] op_sel_hi:[1,0]
	v_pk_mul_f32 v[16:17], v[116:117], s[28:29] op_sel_hi:[1,0]
	v_mov_b32_e32 v8, v2
	v_mov_b32_e32 v9, v2
	v_cvt_pk_fp8_f32 v8, v12, v13
	v_cvt_pk_fp8_f32 v9, v16, v17
	v_pk_mul_f32 v[12:13], v[122:123], s[28:29] op_sel_hi:[1,0]
	v_pk_mul_f32 v[16:17], v[118:119], s[28:29] op_sel_hi:[1,0]
	v_cvt_pk_fp8_f32 v8, v12, v13 op_sel:[0,0,1]
	v_cvt_pk_fp8_f32 v9, v16, v17 op_sel:[0,0,1]
	s_mov_b64 s[28:29], 0

.LBB0_311:
	v_lshl_add_u64 v[6:7], v[6:7], 0, s[28:29]
	v_lshl_add_u64 v[6:7], v[6:7], 0, s[16:17]
	v_lshl_add_u64 v[6:7], v[6:7], 0, v[4:5]
	s_and_b64 vcc, exec, s[6:7]
	s_mov_b64 s[28:29], -1
	v_subrev_u32_e32 v6, s10, v6
	global_store_dwordx2 v6, v[8:9], s[10:11] offset:128
	s_cbranch_vccnz .LBB0_313
	s_mov_b32 s28, 0x3e800000
	v_pk_mul_f32 v[6:7], v[48:49], s[28:29] op_sel_hi:[1,0]
	v_pk_mul_f32 v[12:13], v[44:45], s[28:29] op_sel_hi:[1,0]
	v_mov_b32_e32 v8, v2
	v_mov_b32_e32 v9, v2
	v_cvt_pk_fp8_f32 v8, v6, v7
	v_cvt_pk_fp8_f32 v9, v12, v13
	v_pk_mul_f32 v[6:7], v[50:51], s[28:29] op_sel_hi:[1,0]
	v_pk_mul_f32 v[12:13], v[46:47], s[28:29] op_sel_hi:[1,0]
	v_cvt_pk_fp8_f32 v8, v6, v7 op_sel:[0,0,1]
	v_cvt_pk_fp8_f32 v9, v12, v13 op_sel:[0,0,1]
	s_mov_b64 s[28:29], 0

.LBB0_317:
	v_add_u32_e32 v6, 0xa0, v14
	v_and_b32_e32 v11, 0x7fffffff, v6
	v_mov_b64_e32 v[6:7], s[10:11]
	v_mad_u64_u32 v[6:7], s[48:49], v11, s21, v[6:7]
	v_lshl_add_u64 v[12:13], v[6:7], 0, s[28:29]
	v_lshl_add_u64 v[12:13], v[12:13], 0, s[16:17]
	v_lshl_add_u64 v[12:13], v[12:13], 0, v[4:5]
	s_and_b64 vcc, exec, s[6:7]
	s_mov_b64 s[28:29], -1
	v_subrev_u32_e32 v12, s10, v12
	global_store_dwordx2 v12, v[8:9], s[10:11]
	s_cbranch_vccnz .LBB0_319
	s_mov_b32 s28, 0x3e800000
	v_pk_mul_f32 v[12:13], v[112:113], s[28:29] op_sel_hi:[1,0]
	v_pk_mul_f32 v[16:17], v[108:109], s[28:29] op_sel_hi:[1,0]
	v_mov_b32_e32 v8, v2
	v_mov_b32_e32 v9, v2
	v_cvt_pk_fp8_f32 v8, v12, v13
	v_cvt_pk_fp8_f32 v9, v16, v17
	v_pk_mul_f32 v[12:13], v[114:115], s[28:29] op_sel_hi:[1,0]
	v_pk_mul_f32 v[16:17], v[110:111], s[28:29] op_sel_hi:[1,0]
	v_cvt_pk_fp8_f32 v8, v12, v13 op_sel:[0,0,1]
	v_cvt_pk_fp8_f32 v9, v16, v17 op_sel:[0,0,1]
	s_mov_b64 s[28:29], 0

.LBB0_323:
	v_lshl_add_u64 v[6:7], v[6:7], 0, s[28:29]
	v_lshl_add_u64 v[6:7], v[6:7], 0, s[16:17]
	v_lshl_add_u64 v[6:7], v[6:7], 0, v[4:5]
	s_and_b64 vcc, exec, s[6:7]
	s_mov_b64 s[28:29], -1
	v_subrev_u32_e32 v6, s10, v6
	global_store_dwordx2 v6, v[8:9], s[10:11] offset:128
	s_cbranch_vccnz .LBB0_325
	s_mov_b32 s28, 0x3e800000
	v_pk_mul_f32 v[6:7], v[40:41], s[28:29] op_sel_hi:[1,0]
	v_pk_mul_f32 v[12:13], v[36:37], s[28:29] op_sel_hi:[1,0]
	v_mov_b32_e32 v8, v2
	v_mov_b32_e32 v9, v2
	v_cvt_pk_fp8_f32 v8, v6, v7
	v_cvt_pk_fp8_f32 v9, v12, v13
	v_pk_mul_f32 v[6:7], v[42:43], s[28:29] op_sel_hi:[1,0]
	v_pk_mul_f32 v[12:13], v[38:39], s[28:29] op_sel_hi:[1,0]
	v_cvt_pk_fp8_f32 v8, v6, v7 op_sel:[0,0,1]
	v_cvt_pk_fp8_f32 v9, v12, v13 op_sel:[0,0,1]
	s_mov_b64 s[28:29], 0

.LBB0_329:
	v_add_u32_e32 v6, 0xb0, v14
	v_and_b32_e32 v11, 0x7fffffff, v6
	v_mov_b64_e32 v[6:7], s[10:11]
	v_mad_u64_u32 v[6:7], s[48:49], v11, s21, v[6:7]
	v_lshl_add_u64 v[12:13], v[6:7], 0, s[28:29]
	v_lshl_add_u64 v[12:13], v[12:13], 0, s[16:17]
	v_lshl_add_u64 v[12:13], v[12:13], 0, v[4:5]
	s_and_b64 vcc, exec, s[6:7]
	s_mov_b64 s[6:7], -1
	v_subrev_u32_e32 v12, s10, v12
	global_store_dwordx2 v12, v[8:9], s[10:11]
	s_cbranch_vccnz .LBB0_331
	s_mov_b32 s6, 0x3e800000
	v_pk_mul_f32 v[12:13], v[104:105], s[6:7] op_sel_hi:[1,0]
	v_pk_mul_f32 v[16:17], v[100:101], s[6:7] op_sel_hi:[1,0]
	v_mov_b32_e32 v8, v2
	v_mov_b32_e32 v9, v2
	v_cvt_pk_fp8_f32 v8, v12, v13
	v_cvt_pk_fp8_f32 v9, v16, v17
	v_pk_mul_f32 v[12:13], v[106:107], s[6:7] op_sel_hi:[1,0]
	v_pk_mul_f32 v[16:17], v[102:103], s[6:7] op_sel_hi:[1,0]
	v_cvt_pk_fp8_f32 v8, v12, v13 op_sel:[0,0,1]
	v_cvt_pk_fp8_f32 v9, v16, v17 op_sel:[0,0,1]
	s_mov_b64 s[6:7], 0

.LBB0_335:
	v_lshl_add_u64 v[6:7], v[6:7], 0, s[0:1]
	v_lshl_add_u64 v[6:7], v[6:7], 0, s[16:17]
	v_lshl_add_u64 v[4:5], v[6:7], 0, v[4:5]
	v_subrev_u32_e32 v4, s10, v4
	global_store_dwordx2 v4, v[8:9], s[10:11] offset:128
